# peersel middle stage: 60-comparator sorting network for the two sort16 (was 80-comparator bitonic), order-preserving key with one v_bitop3
# speedup vs baseline: 1.0296x; 1.0091x over previous
; #define MFMA16(a, b, c) __builtin_amdgcn_mfma_f32_16x16x32_bf16((a), (b), (c), 0, 0, 0)
; DI void peer_select_unit(const Params& p, int unit, char* lds, const bf16x8 (&kb)[4][4]) {
;     ...
;     const int set = wid >> 1, kh = wid & 1;
;     bf16x8 qa[2][4];
; #pragma unroll
;     for (int mt = 0; mt < 2; ++mt)
; #pragma unroll
;       for (int kk = 0; kk < 4; ++kk) qa[mt][kk] = *(const bf16x8*)(qy + (size_t)(t0 + 16 * mt + fr) * 2048 + h * 256 + set * 128 + kk * 32 + fq * 8);
; #pragma unroll
;     for (int mt = 0; mt < 2; ++mt)
; #pragma unroll
;       for (int nj = 0; nj < 4; ++nj) {
;         f32x4 d = {0.f, 0.f, 0.f, 0.f};
; #pragma unroll
;         for (int kk = 0; kk < 4; ++kk) d = MFMA16(qa[mt][kk], kb[nj][kk], d);
; #pragma unroll
;         for (int r = 0; r < 4; ++r) sc[(set * 32 + 16 * mt + 4 * fq + r) * 132 + 64 * kh + 16 * nj + fr] = d[r];
;       }
;   }
;   __syncthreads();
.LBB0_1652:
	v_lshlrev_b32_e32 v64, 2, v72
	v_mov_b32_e32 v66, v206
	v_and_b32_e32 v73, 7, v72
	v_and_b32_e32 v74, 0xffffffe0, v64
	v_lshlrev_b32_e32 v64, 9, v73
	v_and_or_b32 v84, v66, 15, v74
	v_and_b32_e32 v70, 0xffffff80, v66
	v_bfe_u32 v67, v66, 4, 2
	v_lshl_add_u64 v[68:69], s[58:59], 0, v[64:65]
	v_ashrrev_i32_e32 v71, 31, v70
	v_or_b32_e32 v90, 16, v84
	v_lshl_add_u64 v[68:69], v[70:71], 1, v[68:69]
	v_lshlrev_b32_e32 v64, 4, v67
	v_ashrrev_i32_e32 v85, 31, v84
	v_ashrrev_i32_e32 v91, 31, v90
	v_lshl_add_u64 v[88:89], v[68:69], 0, v[64:65]
	v_lshlrev_b64 v[68:69], 12, v[84:85]
	v_lshlrev_b64 v[90:91], 12, v[90:91]
	v_lshl_add_u64 v[116:117], v[88:89], 0, v[68:69]
	v_lshl_add_u64 v[120:121], v[88:89], 0, v[90:91]
	s_barrier
	s_waitcnt vmcnt(0)
	v_mov_b32_e32 v68, v148
	v_mov_b32_e32 v69, v149
	v_mov_b32_e32 v70, v150
	v_mov_b32_e32 v71, v151
	v_mov_b32_e32 v76, v152
	v_mov_b32_e32 v77, v153
	v_mov_b32_e32 v78, v154
	v_mov_b32_e32 v79, v155
	v_mov_b32_e32 v92, v156
	v_mov_b32_e32 v93, v157
	v_mov_b32_e32 v94, v158
	v_mov_b32_e32 v95, v159
	v_mov_b32_e32 v96, v160
	v_mov_b32_e32 v97, v161
	v_mov_b32_e32 v98, v162
	v_mov_b32_e32 v99, v163
	v_ashrrev_i32_e32 v75, 2, v66
	v_and_b32_e32 v64, 0x4f, v66
	v_lshlrev_b32_e32 v64, 2, v64
	s_mov_b64 s[20:21], -1
	s_mov_b32 s69, 0
	v_mfma_f32_16x16x32_bf16 v[80:83], v[68:71], v[0:3], 0
	v_mfma_f32_16x16x32_bf16 v[84:87], v[68:71], v[56:59], 0
	v_mfma_f32_16x16x32_bf16 v[88:91], v[68:71], v[24:27], 0
	v_mfma_f32_16x16x32_bf16 v[68:71], v[68:71], v[44:47], 0
	v_mfma_f32_16x16x32_bf16 v[100:103], v[92:95], v[0:3], 0
	v_mfma_f32_16x16x32_bf16 v[104:107], v[92:95], v[56:59], 0
	v_mfma_f32_16x16x32_bf16 v[108:111], v[92:95], v[24:27], 0
	v_mfma_f32_16x16x32_bf16 v[80:83], v[76:79], v[4:7], v[80:83]
	v_mfma_f32_16x16x32_bf16 v[84:87], v[76:79], v[16:19], v[84:87]
	v_mfma_f32_16x16x32_bf16 v[88:91], v[76:79], v[28:31], v[88:91]
	v_mfma_f32_16x16x32_bf16 v[68:71], v[76:79], v[48:51], v[68:71]
	v_mfma_f32_16x16x32_bf16 v[76:79], v[96:99], v[4:7], v[100:103]
	v_mfma_f32_16x16x32_bf16 v[100:103], v[96:99], v[16:19], v[104:107]
	v_mfma_f32_16x16x32_bf16 v[104:107], v[96:99], v[28:31], v[108:111]
	s_nop 2
	s_nop 1
	v_mov_b32_e32 v108, v164
	v_mov_b32_e32 v109, v165
	v_mov_b32_e32 v110, v166
	v_mov_b32_e32 v111, v167
	v_mov_b32_e32 v112, v168
	v_mov_b32_e32 v113, v169
	v_mov_b32_e32 v114, v170
	v_mov_b32_e32 v115, v171
	v_mov_b32_e32 v116, v172
	v_mov_b32_e32 v117, v173
	v_mov_b32_e32 v118, v174
	v_mov_b32_e32 v119, v175
	s_nop 1
	v_mfma_f32_16x16x32_bf16 v[80:83], v[108:111], v[8:11], v[80:83]
	v_mfma_f32_16x16x32_bf16 v[84:87], v[108:111], v[20:23], v[84:87]
	v_mfma_f32_16x16x32_bf16 v[88:91], v[108:111], v[32:35], v[88:91]
	v_mfma_f32_16x16x32_bf16 v[68:71], v[108:111], v[52:55], v[68:71]
	s_nop 3
	v_mov_b32_e32 v108, v178
	v_mov_b32_e32 v109, v179
	v_mov_b32_e32 v110, v180
	v_mov_b32_e32 v111, v181
	v_add_u32_e32 v184, s90, v72
	v_min_u32_e32 v184, s68, v184
	v_lshrrev_b32_e32 v185, 3, v184
	v_lshlrev_b32_e32 v185, 17, v185
	v_and_b32_e32 v184, 7, v184
	v_lshl_or_b32 v184, v184, 9, v185
	v_mov_b32_e32 v185, 0
	v_lshl_add_u64 v[184:185], v[182:183], 0, v[184:185]
	v_mov_b32_e32 v186, 0x10000
	v_mov_b32_e32 v187, 0
	v_lshl_add_u64 v[186:187], v[184:185], 0, v[186:187]
	global_load_dwordx4 v[148:151], v[184:185], off
	global_load_dwordx4 v[152:155], v[184:185], off offset:64
	global_load_dwordx4 v[156:159], v[186:187], off
	global_load_dwordx4 v[160:163], v[186:187], off offset:64
	global_load_dwordx4 v[164:167], v[184:185], off offset:128
	global_load_dwordx4 v[168:171], v[184:185], off offset:192
	global_load_dwordx4 v[172:175], v[186:187], off offset:128
	global_load_dwordx4 v[178:181], v[186:187], off offset:192
	s_nop 1
	v_mfma_f32_16x16x32_bf16 v[80:83], v[112:115], v[12:15], v[80:83]
	v_mfma_f32_16x16x32_bf16 v[84:87], v[112:115], v[40:43], v[84:87]
	v_mfma_f32_16x16x32_bf16 v[88:91], v[112:115], v[36:39], v[88:91]
	v_mfma_f32_16x16x32_bf16 v[68:71], v[112:115], v[60:63], v[68:71]
	v_and_b32_e32 v112, 0xfffffe0, v75
	v_lshl_or_b32 v67, v67, 2, v112
	v_mul_lo_u32 v67, v67, s2
	v_add3_u32 v64, v146, v67, v64
	v_add_u32_e32 v67, 0x400, v64
	s_nop 0
	ds_write2_b32 v64, v80, v84 offset1:16
	ds_write2_b32 v64, v81, v85 offset0:132 offset1:148
	ds_write2_b32 v67, v82, v86 offset0:8 offset1:24
	ds_write2_b32 v67, v83, v87 offset0:140 offset1:156
	ds_write2_b32 v64, v88, v68 offset0:32 offset1:48
	v_mfma_f32_16x16x32_bf16 v[80:83], v[92:95], v[44:47], 0
	ds_write2_b32 v64, v89, v69 offset0:164 offset1:180
	ds_write2_b32 v67, v90, v70 offset0:40 offset1:56
	ds_write2_b32 v67, v91, v71 offset0:172 offset1:188
	v_add_u32_e32 v67, 0x2000, v64
	v_add_u32_e32 v64, 0x2400, v64
	v_mfma_f32_16x16x32_bf16 v[68:71], v[96:99], v[48:51], v[80:83]
	v_mfma_f32_16x16x32_bf16 v[76:79], v[116:119], v[8:11], v[76:79]
	v_mfma_f32_16x16x32_bf16 v[100:103], v[116:119], v[20:23], v[100:103]
	v_mfma_f32_16x16x32_bf16 v[104:107], v[116:119], v[32:35], v[104:107]
	v_mfma_f32_16x16x32_bf16 v[68:71], v[116:119], v[52:55], v[68:71]
	v_mfma_f32_16x16x32_bf16 v[76:79], v[108:111], v[12:15], v[76:79]
	v_mfma_f32_16x16x32_bf16 v[100:103], v[108:111], v[40:43], v[100:103]
	s_nop 7
	ds_write2_b32 v67, v76, v100 offset0:64 offset1:80
	ds_write2_b32 v67, v77, v101 offset0:196 offset1:212
	v_mfma_f32_16x16x32_bf16 v[104:107], v[108:111], v[36:39], v[104:107]
	ds_write2_b32 v64, v78, v102 offset0:72 offset1:88
	ds_write2_b32 v64, v79, v103 offset0:204 offset1:220
	v_mfma_f32_16x16x32_bf16 v[68:71], v[108:111], v[60:63], v[68:71]
	s_nop 7
	ds_write2_b32 v67, v104, v68 offset0:96 offset1:112
	ds_write2_b32 v67, v105, v69 offset0:228 offset1:244
	ds_write2_b32 v64, v106, v70 offset0:104 offset1:120
	ds_write2_b32 v64, v107, v71 offset0:236 offset1:252
	v_lshrrev_b32_e32 v236, 2, v66
	v_and_b32_e32 v237, 3, v66
	v_mul_u32_u24_e32 v238, 0x210, v236
	v_add_u32_e32 v238, v146, v238
	v_lshl_add_u32 v239, v237, 6, v238
	s_waitcnt lgkmcnt(0)
	s_barrier
; DI unsigned ordkey(float f) { const unsigned u = __float_as_uint(f); return (u & 0x80000000u) ? ~u : (u | 0x80000000u); }
; DI void peer_select_unit(const Params& p, int unit, char* lds, const bf16x8 (&kb)[4][4]) {
;     ...
;     const int rr = pass * 32 + (tid >> 3), part = tid & 7;
;     unsigned a[16], bq[16];
;     const float* srow = sc + rr * 132 + 16 * part;
; #pragma unroll
;     for (int j = 0; j < 4; ++j) {
;       const f32x4 v = *(const f32x4*)(srow + 4 * j);
; #pragma unroll
;       for (int e = 0; e < 4; ++e) a[4 * j + e] = (ordkey(v[e]) & ~127u) | (unsigned)(127 - (16 * part + 4 * j + e));
;     }
	ds_read_b128 v[124:127], v239 offset:0
	ds_read_b128 v[128:131], v239 offset:16
	ds_read_b128 v[132:135], v239 offset:32
	ds_read_b128 v[136:139], v239 offset:48
	ds_read_b128 v[212:215], v239 offset:256
	ds_read_b128 v[216:219], v239 offset:272
	ds_read_b128 v[220:223], v239 offset:288
	ds_read_b128 v[224:227], v239 offset:304
	v_lshlrev_b32_e32 v240, 4, v237
	v_sub_u32_e32 v241, 0x7f, v240
	v_sub_u32_e32 v242, 63, v240
	v_mov_b32_e32 v243, 0xffffff80
	v_bfrev_b32_e32 v240, 1
	s_waitcnt lgkmcnt(7)
	v_ashrrev_i32_e32 v122, 31, v124
	v_bitop3_b32 v124, v124, v122, v240 bitop3:0x1e
	v_and_or_b32 v124, v124, v243, v241
	v_ashrrev_i32_e32 v123, 31, v125
	v_bitop3_b32 v125, v125, v123, v240 bitop3:0x1e
	v_and_or_b32 v125, v125, v243, v241
	v_subrev_u32_e32 v125, 1, v125
	v_ashrrev_i32_e32 v140, 31, v126
	v_bitop3_b32 v126, v126, v140, v240 bitop3:0x1e
	v_and_or_b32 v126, v126, v243, v241
	v_subrev_u32_e32 v126, 2, v126
	v_ashrrev_i32_e32 v141, 31, v127
	v_bitop3_b32 v127, v127, v141, v240 bitop3:0x1e
	v_and_or_b32 v127, v127, v243, v241
	v_subrev_u32_e32 v127, 3, v127
	s_waitcnt lgkmcnt(6)
	v_ashrrev_i32_e32 v142, 31, v128
	v_bitop3_b32 v128, v128, v142, v240 bitop3:0x1e
	v_and_or_b32 v128, v128, v243, v241
	v_subrev_u32_e32 v128, 4, v128
	v_ashrrev_i32_e32 v143, 31, v129
	v_bitop3_b32 v129, v129, v143, v240 bitop3:0x1e
	v_and_or_b32 v129, v129, v243, v241
	v_subrev_u32_e32 v129, 5, v129
	v_ashrrev_i32_e32 v144, 31, v130
	v_bitop3_b32 v130, v130, v144, v240 bitop3:0x1e
	v_and_or_b32 v130, v130, v243, v241
	v_subrev_u32_e32 v130, 6, v130
	v_ashrrev_i32_e32 v145, 31, v131
	v_bitop3_b32 v131, v131, v145, v240 bitop3:0x1e
	v_and_or_b32 v131, v131, v243, v241
	v_subrev_u32_e32 v131, 7, v131
	s_waitcnt lgkmcnt(5)
	v_ashrrev_i32_e32 v194, 31, v132
	v_bitop3_b32 v132, v132, v194, v240 bitop3:0x1e
	v_and_or_b32 v132, v132, v243, v241
	v_subrev_u32_e32 v132, 8, v132
	v_ashrrev_i32_e32 v195, 31, v133
	v_bitop3_b32 v133, v133, v195, v240 bitop3:0x1e
	v_and_or_b32 v133, v133, v243, v241
	v_subrev_u32_e32 v133, 9, v133
	v_ashrrev_i32_e32 v196, 31, v134
	v_bitop3_b32 v134, v134, v196, v240 bitop3:0x1e
	v_and_or_b32 v134, v134, v243, v241
	v_subrev_u32_e32 v134, 10, v134
	v_ashrrev_i32_e32 v197, 31, v135
	v_bitop3_b32 v135, v135, v197, v240 bitop3:0x1e
	v_and_or_b32 v135, v135, v243, v241
	v_subrev_u32_e32 v135, 11, v135
	s_waitcnt lgkmcnt(4)
	v_ashrrev_i32_e32 v198, 31, v136
	v_bitop3_b32 v136, v136, v198, v240 bitop3:0x1e
	v_and_or_b32 v136, v136, v243, v241
	v_subrev_u32_e32 v136, 12, v136
	v_ashrrev_i32_e32 v199, 31, v137
	v_bitop3_b32 v137, v137, v199, v240 bitop3:0x1e
	v_and_or_b32 v137, v137, v243, v241
	v_subrev_u32_e32 v137, 13, v137
	v_ashrrev_i32_e32 v200, 31, v138
	v_bitop3_b32 v138, v138, v200, v240 bitop3:0x1e
	v_and_or_b32 v138, v138, v243, v241
	v_subrev_u32_e32 v138, 14, v138
	v_ashrrev_i32_e32 v201, 31, v139
	v_bitop3_b32 v139, v139, v201, v240 bitop3:0x1e
	v_and_or_b32 v139, v139, v243, v241
	v_subrev_u32_e32 v139, 15, v139
	s_waitcnt lgkmcnt(3)
	v_ashrrev_i32_e32 v202, 31, v212
	v_bitop3_b32 v212, v212, v202, v240 bitop3:0x1e
	v_and_or_b32 v212, v212, v243, v242
	v_ashrrev_i32_e32 v203, 31, v213
	v_bitop3_b32 v213, v213, v203, v240 bitop3:0x1e
	v_and_or_b32 v213, v213, v243, v242
	v_subrev_u32_e32 v213, 1, v213
	v_ashrrev_i32_e32 v204, 31, v214
	v_bitop3_b32 v214, v214, v204, v240 bitop3:0x1e
	v_and_or_b32 v214, v214, v243, v242
	v_subrev_u32_e32 v214, 2, v214
	v_ashrrev_i32_e32 v205, 31, v215
	v_bitop3_b32 v215, v215, v205, v240 bitop3:0x1e
	v_and_or_b32 v215, v215, v243, v242
	v_subrev_u32_e32 v215, 3, v215
	s_waitcnt lgkmcnt(2)
	v_ashrrev_i32_e32 v122, 31, v216
	v_bitop3_b32 v216, v216, v122, v240 bitop3:0x1e
	v_and_or_b32 v216, v216, v243, v242
	v_subrev_u32_e32 v216, 4, v216
	v_ashrrev_i32_e32 v123, 31, v217
	v_bitop3_b32 v217, v217, v123, v240 bitop3:0x1e
	v_and_or_b32 v217, v217, v243, v242
	v_subrev_u32_e32 v217, 5, v217
	v_ashrrev_i32_e32 v140, 31, v218
	v_bitop3_b32 v218, v218, v140, v240 bitop3:0x1e
	v_and_or_b32 v218, v218, v243, v242
	v_subrev_u32_e32 v218, 6, v218
	v_ashrrev_i32_e32 v141, 31, v219
	v_bitop3_b32 v219, v219, v141, v240 bitop3:0x1e
	v_and_or_b32 v219, v219, v243, v242
	v_subrev_u32_e32 v219, 7, v219
	s_waitcnt lgkmcnt(1)
	v_ashrrev_i32_e32 v142, 31, v220
	v_bitop3_b32 v220, v220, v142, v240 bitop3:0x1e
	v_and_or_b32 v220, v220, v243, v242
	v_subrev_u32_e32 v220, 8, v220
	v_ashrrev_i32_e32 v143, 31, v221
	v_bitop3_b32 v221, v221, v143, v240 bitop3:0x1e
	v_and_or_b32 v221, v221, v243, v242
	v_subrev_u32_e32 v221, 9, v221
	v_ashrrev_i32_e32 v144, 31, v222
	v_bitop3_b32 v222, v222, v144, v240 bitop3:0x1e
	v_and_or_b32 v222, v222, v243, v242
	v_subrev_u32_e32 v222, 10, v222
	v_ashrrev_i32_e32 v145, 31, v223
	v_bitop3_b32 v223, v223, v145, v240 bitop3:0x1e
	v_and_or_b32 v223, v223, v243, v242
	v_subrev_u32_e32 v223, 11, v223
	s_waitcnt lgkmcnt(0)
; DI unsigned ordkey(float f) { const unsigned u = __float_as_uint(f); return (u & 0x80000000u) ? ~u : (u | 0x80000000u); }
; #define CE_DESC(x, y) do { const unsigned mx_ = (x) > (y) ? (x) : (y); const unsigned mn_ = (x) > (y) ? (y) : (x); (x) = mx_; (y) = mn_; } while (0)
; DI void sort16_desc(unsigned (&a)[16]) {
; #pragma unroll
;   for (int k = 2; k <= 16; k <<= 1)
; #pragma unroll
;     for (int j = k >> 1; j > 0; j >>= 1)
; #pragma unroll
;       for (int i = 0; i < 16; ++i) {
;         const int l = i ^ j;
;         if (l > i) { if ((i & k) == 0) CE_DESC(a[i], a[l]); else CE_DESC(a[l], a[i]); }
;       }
; }
; DI void peer_select_unit(const Params& p, int unit, char* lds, const bf16x8 (&kb)[4][4]) {
;     ...
;       for (int e = 0; e < 4; ++e) a[4 * j + e] = (ordkey(v[e]) & ~127u) | (unsigned)(127 - (16 * part + 4 * j + e));
;     }
;     sort16_desc(a);
	v_ashrrev_i32_e32 v194, 31, v224
	v_bitop3_b32 v224, v224, v194, v240 bitop3:0x1e
	v_and_or_b32 v224, v224, v243, v242
	v_subrev_u32_e32 v224, 12, v224
	v_ashrrev_i32_e32 v195, 31, v225
	v_bitop3_b32 v225, v225, v195, v240 bitop3:0x1e
	v_and_or_b32 v225, v225, v243, v242
	v_subrev_u32_e32 v225, 13, v225
	v_ashrrev_i32_e32 v196, 31, v226
	v_bitop3_b32 v226, v226, v196, v240 bitop3:0x1e
	v_and_or_b32 v226, v226, v243, v242
	v_subrev_u32_e32 v226, 14, v226
	v_ashrrev_i32_e32 v197, 31, v227
	v_bitop3_b32 v227, v227, v197, v240 bitop3:0x1e
	v_and_or_b32 v227, v227, v243, v242
	v_subrev_u32_e32 v227, 15, v227
	v_max_u32_e32 v198, v124, v137
	v_min_u32_e32 v199, v124, v137
	v_max_u32_e32 v200, v212, v225
	v_min_u32_e32 v201, v212, v225
	v_max_u32_e32 v202, v125, v136
	v_min_u32_e32 v203, v125, v136
	v_max_u32_e32 v204, v213, v224
	v_min_u32_e32 v205, v213, v224
	v_max_u32_e32 v122, v126, v139
	v_min_u32_e32 v123, v126, v139
	v_max_u32_e32 v140, v214, v227
	v_min_u32_e32 v141, v214, v227
	v_max_u32_e32 v142, v127, v138
	v_min_u32_e32 v143, v127, v138
	v_max_u32_e32 v144, v215, v226
	v_min_u32_e32 v145, v215, v226
	v_max_u32_e32 v194, v128, v132
	v_min_u32_e32 v195, v128, v132
	v_max_u32_e32 v196, v216, v220
	v_min_u32_e32 v197, v216, v220
	v_max_u32_e32 v124, v129, v130
	v_min_u32_e32 v137, v129, v130
	v_max_u32_e32 v212, v217, v218
	v_min_u32_e32 v225, v217, v218
	v_max_u32_e32 v125, v131, v135
	v_min_u32_e32 v136, v131, v135
	v_max_u32_e32 v213, v219, v223
	v_min_u32_e32 v224, v219, v223
	v_max_u32_e32 v126, v133, v134
	v_min_u32_e32 v139, v133, v134
	v_max_u32_e32 v214, v221, v222
	v_min_u32_e32 v227, v221, v222
	v_max_u32_e32 v127, v198, v124
	v_min_u32_e32 v138, v198, v124
	v_max_u32_e32 v215, v200, v212
	v_min_u32_e32 v226, v200, v212
	v_max_u32_e32 v128, v202, v125
	v_min_u32_e32 v132, v202, v125
	v_max_u32_e32 v216, v204, v213
	v_min_u32_e32 v220, v204, v213
	v_max_u32_e32 v129, v122, v126
	v_min_u32_e32 v130, v122, v126
	v_max_u32_e32 v217, v140, v214
	v_min_u32_e32 v218, v140, v214
	v_max_u32_e32 v131, v142, v194
	v_min_u32_e32 v135, v142, v194
	v_max_u32_e32 v219, v144, v196
	v_min_u32_e32 v223, v144, v196
	v_max_u32_e32 v133, v137, v199
	v_min_u32_e32 v134, v137, v199
	v_max_u32_e32 v221, v225, v201
	v_min_u32_e32 v222, v225, v201
	v_max_u32_e32 v198, v195, v143
	v_min_u32_e32 v124, v195, v143
	v_max_u32_e32 v200, v197, v145
	v_min_u32_e32 v212, v197, v145
	v_max_u32_e32 v202, v139, v123
	v_min_u32_e32 v125, v139, v123
	v_max_u32_e32 v204, v227, v141
	v_min_u32_e32 v213, v227, v141
	v_max_u32_e32 v122, v136, v203
	v_min_u32_e32 v126, v136, v203
	v_max_u32_e32 v140, v224, v205
	v_min_u32_e32 v214, v224, v205
	v_max_u32_e32 v142, v127, v128
	v_min_u32_e32 v194, v127, v128
	v_max_u32_e32 v144, v215, v216
	v_min_u32_e32 v196, v215, v216
	v_max_u32_e32 v137, v129, v131
	v_min_u32_e32 v199, v129, v131
	v_max_u32_e32 v225, v217, v219
	v_min_u32_e32 v201, v217, v219
	v_max_u32_e32 v195, v135, v138
	v_min_u32_e32 v143, v135, v138
	v_max_u32_e32 v197, v223, v226
	v_min_u32_e32 v145, v223, v226
	v_max_u32_e32 v139, v133, v198
	v_min_u32_e32 v123, v133, v198
	v_max_u32_e32 v227, v221, v200
	v_min_u32_e32 v141, v221, v200
	v_max_u32_e32 v136, v132, v130
	v_min_u32_e32 v203, v132, v130
	v_max_u32_e32 v224, v220, v218
	v_min_u32_e32 v205, v220, v218
	v_max_u32_e32 v127, v202, v122
	v_min_u32_e32 v128, v202, v122
	v_max_u32_e32 v215, v204, v140
	v_min_u32_e32 v216, v204, v140
	v_max_u32_e32 v129, v126, v134
	v_min_u32_e32 v131, v126, v134
	v_max_u32_e32 v217, v214, v222
	v_min_u32_e32 v219, v214, v222
	v_max_u32_e32 v135, v124, v125
	v_min_u32_e32 v138, v124, v125
	v_max_u32_e32 v223, v212, v213
	v_min_u32_e32 v226, v212, v213
	v_max_u32_e32 v133, v142, v137
	v_min_u32_e32 v198, v142, v137
	v_max_u32_e32 v221, v144, v225
	v_min_u32_e32 v200, v144, v225
	v_max_u32_e32 v132, v194, v199
	v_min_u32_e32 v130, v194, v199
	v_max_u32_e32 v220, v196, v201
	v_min_u32_e32 v218, v196, v201
	v_max_u32_e32 v202, v195, v127
	v_min_u32_e32 v122, v195, v127
	v_max_u32_e32 v204, v197, v215
	v_min_u32_e32 v140, v197, v215
	v_max_u32_e32 v126, v143, v128
	v_min_u32_e32 v134, v143, v128
	v_max_u32_e32 v214, v145, v216
	v_min_u32_e32 v222, v145, v216
	v_max_u32_e32 v124, v139, v136
	v_min_u32_e32 v125, v139, v136
	v_max_u32_e32 v212, v227, v224
	v_min_u32_e32 v213, v227, v224
	v_max_u32_e32 v142, v123, v203
	v_min_u32_e32 v137, v123, v203
	v_max_u32_e32 v144, v141, v205
	v_min_u32_e32 v225, v141, v205
	v_max_u32_e32 v194, v129, v135
	v_min_u32_e32 v199, v129, v135
	v_max_u32_e32 v196, v217, v223
	v_min_u32_e32 v201, v217, v223
	v_max_u32_e32 v195, v131, v138
	v_min_u32_e32 v127, v131, v138
	v_max_u32_e32 v197, v219, v226
	v_min_u32_e32 v215, v219, v226
	v_max_u32_e32 v143, v132, v198
	v_min_u32_e32 v128, v132, v198
	v_max_u32_e32 v145, v220, v200
	v_min_u32_e32 v216, v220, v200
	v_max_u32_e32 v139, v130, v194
	v_min_u32_e32 v136, v130, v194
	v_max_u32_e32 v227, v218, v196
	v_min_u32_e32 v224, v218, v196
	v_max_u32_e32 v123, v202, v124
	v_min_u32_e32 v203, v202, v124
	v_max_u32_e32 v141, v204, v212
	v_min_u32_e32 v205, v204, v212
	v_max_u32_e32 v129, v126, v125
	v_min_u32_e32 v135, v126, v125
	v_max_u32_e32 v217, v214, v213
	v_min_u32_e32 v223, v214, v213
	v_max_u32_e32 v131, v142, v122
	v_min_u32_e32 v138, v142, v122
	v_max_u32_e32 v219, v144, v140
	v_min_u32_e32 v226, v144, v140
	v_max_u32_e32 v132, v137, v134
	v_min_u32_e32 v198, v137, v134
	v_max_u32_e32 v220, v225, v222
	v_min_u32_e32 v200, v225, v222
	v_max_u32_e32 v130, v195, v199
	v_min_u32_e32 v194, v195, v199
	v_max_u32_e32 v218, v197, v201
	v_min_u32_e32 v196, v197, v201
	v_max_u32_e32 v202, v143, v123
; #define CE_DESC(x, y) do { const unsigned mx_ = (x) > (y) ? (x) : (y); const unsigned mn_ = (x) > (y) ? (y) : (x); (x) = mx_; (y) = mn_; } while (0)
; DI void sort16_desc(unsigned (&a)[16]) {
; #pragma unroll
;   for (int k = 2; k <= 16; k <<= 1)
; #pragma unroll
;     for (int j = k >> 1; j > 0; j >>= 1)
; #pragma unroll
;       for (int i = 0; i < 16; ++i) {
;         const int l = i ^ j;
;         if (l > i) { if ((i & k) == 0) CE_DESC(a[i], a[l]); else CE_DESC(a[l], a[i]); }
;       }
; }
; DI void merge16_desc(unsigned (&a)[16], const unsigned (&b)[16]) {
; #pragma unroll
;   for (int i = 0; i < 16; ++i) a[i] = a[i] > b[15 - i] ? a[i] : b[15 - i];
; #pragma unroll
;   for (int j = 8; j > 0; j >>= 1)
; #pragma unroll
;     for (int i = 0; i < 16; ++i) if ((i & j) == 0) CE_DESC(a[i], a[i + j]);
; }
; template <int CTRL> DI void dpp16(unsigned (&b)[16], const unsigned (&a)[16]) {
; #pragma unroll
;   for (int s = 0; s < 16; ++s) b[s] = (unsigned)__builtin_amdgcn_update_dpp(0, (int)a[s], CTRL, 0xF, 0xF, true);
; }
; DI void peer_select_unit(const Params& p, int unit, char* lds, const bf16x8 (&kb)[4][4]) {
;     ...
;     sort16_desc(a);
;     dpp16<0xB1>(bq, a); merge16_desc(a, bq);
;     dpp16<0x4E>(bq, a); merge16_desc(a, bq);
	v_min_u32_e32 v124, v143, v123
	v_max_u32_e32 v204, v145, v141
	v_min_u32_e32 v212, v145, v141
	v_max_u32_e32 v126, v128, v203
	v_min_u32_e32 v125, v128, v203
	v_max_u32_e32 v214, v216, v205
	v_min_u32_e32 v213, v216, v205
	v_max_u32_e32 v142, v129, v131
	v_min_u32_e32 v122, v129, v131
	v_max_u32_e32 v144, v217, v219
	v_min_u32_e32 v140, v217, v219
	v_max_u32_e32 v137, v135, v138
	v_min_u32_e32 v134, v135, v138
	v_max_u32_e32 v225, v223, v226
	v_min_u32_e32 v222, v223, v226
	v_max_u32_e32 v195, v132, v130
	v_min_u32_e32 v199, v132, v130
	v_max_u32_e32 v197, v220, v218
	v_min_u32_e32 v201, v220, v218
	v_max_u32_e32 v143, v198, v194
	v_min_u32_e32 v123, v198, v194
	v_max_u32_e32 v145, v200, v196
	v_min_u32_e32 v141, v200, v196
	v_max_u32_e32 v128, v126, v124
	v_min_u32_e32 v203, v126, v124
	v_max_u32_e32 v216, v214, v212
	v_min_u32_e32 v205, v214, v212
	v_max_u32_e32 v129, v139, v125
	v_min_u32_e32 v131, v139, v125
	v_max_u32_e32 v217, v227, v213
	v_min_u32_e32 v219, v227, v213
	v_max_u32_e32 v135, v195, v136
	v_min_u32_e32 v138, v195, v136
	v_max_u32_e32 v223, v197, v224
	v_min_u32_e32 v226, v197, v224
	v_max_u32_e32 v132, v143, v199
	v_min_u32_e32 v130, v143, v199
	v_max_u32_e32 v220, v145, v201
	v_min_u32_e32 v218, v145, v201
	v_max_u32_e32 v198, v129, v142
	v_min_u32_e32 v194, v129, v142
	v_max_u32_e32 v200, v217, v144
	v_min_u32_e32 v196, v217, v144
	v_max_u32_e32 v126, v131, v122
	v_min_u32_e32 v124, v131, v122
	v_max_u32_e32 v214, v219, v140
	v_min_u32_e32 v212, v219, v140
	v_max_u32_e32 v139, v137, v135
	v_min_u32_e32 v125, v137, v135
	v_max_u32_e32 v227, v225, v223
	v_min_u32_e32 v213, v225, v223
	v_max_u32_e32 v195, v134, v138
	v_min_u32_e32 v136, v134, v138
	v_max_u32_e32 v197, v222, v226
	v_min_u32_e32 v224, v222, v226
	v_max_u32_e32 v143, v198, v203
	v_min_u32_e32 v199, v198, v203
	v_max_u32_e32 v145, v200, v205
	v_min_u32_e32 v201, v200, v205
	v_max_u32_e32 v129, v194, v126
	v_min_u32_e32 v142, v194, v126
	v_max_u32_e32 v217, v196, v214
	v_min_u32_e32 v144, v196, v214
	v_max_u32_e32 v131, v139, v124
	v_min_u32_e32 v122, v139, v124
	v_max_u32_e32 v219, v227, v212
	v_min_u32_e32 v140, v227, v212
	v_max_u32_e32 v137, v125, v195
	v_min_u32_e32 v135, v125, v195
	v_max_u32_e32 v225, v213, v197
	v_min_u32_e32 v223, v213, v197
	v_max_u32_e32 v134, v132, v136
	v_min_u32_e32 v138, v132, v136
	v_max_u32_e32 v222, v220, v224
	v_min_u32_e32 v226, v220, v224
	v_max_u32_e32 v198, v142, v131
	v_min_u32_e32 v203, v142, v131
	v_max_u32_e32 v200, v144, v219
	v_min_u32_e32 v205, v144, v219
	v_max_u32_e32 v194, v122, v137
	v_min_u32_e32 v126, v122, v137
	v_max_u32_e32 v196, v140, v225
	v_min_u32_e32 v214, v140, v225
	v_max_u32_e32 v139, v133, v215
	v_max_u32_e32 v124, v202, v141
	v_max_u32_e32 v227, v128, v218
	v_max_u32_e32 v212, v143, v226
	v_max_u32_e32 v125, v199, v222
	v_max_u32_e32 v195, v129, v223
	v_max_u32_e32 v213, v198, v214
	v_max_u32_e32 v197, v203, v196
	v_max_u32_e32 v132, v194, v205
	v_max_u32_e32 v136, v126, v200
	v_max_u32_e32 v220, v135, v217
	v_max_u32_e32 v224, v134, v201
	v_max_u32_e32 v142, v138, v145
	v_max_u32_e32 v131, v130, v216
	v_max_u32_e32 v144, v123, v204
	v_max_u32_e32 v219, v127, v221
	v_max_u32_e32 v122, v139, v132
	v_min_u32_e32 v137, v139, v132
	v_max_u32_e32 v140, v124, v136
	v_min_u32_e32 v225, v124, v136
	v_max_u32_e32 v133, v227, v220
	v_min_u32_e32 v202, v227, v220
	v_max_u32_e32 v128, v212, v224
	v_min_u32_e32 v143, v212, v224
	v_max_u32_e32 v199, v125, v142
	v_min_u32_e32 v129, v125, v142
	v_max_u32_e32 v198, v195, v131
	v_min_u32_e32 v203, v195, v131
	v_max_u32_e32 v194, v213, v144
	v_min_u32_e32 v126, v213, v144
	v_max_u32_e32 v135, v197, v219
	v_min_u32_e32 v134, v197, v219
	v_max_u32_e32 v138, v122, v199
	v_min_u32_e32 v130, v122, v199
	v_max_u32_e32 v123, v140, v198
	v_min_u32_e32 v127, v140, v198
	v_max_u32_e32 v221, v133, v194
	v_min_u32_e32 v204, v133, v194
	v_max_u32_e32 v216, v128, v135
	v_min_u32_e32 v145, v128, v135
	v_max_u32_e32 v201, v137, v129
	v_min_u32_e32 v217, v137, v129
	v_max_u32_e32 v200, v225, v203
	v_min_u32_e32 v205, v225, v203
	v_max_u32_e32 v196, v202, v126
	v_min_u32_e32 v214, v202, v126
	v_max_u32_e32 v223, v143, v134
	v_min_u32_e32 v222, v143, v134
	v_max_u32_e32 v226, v138, v221
	v_min_u32_e32 v218, v138, v221
	v_max_u32_e32 v141, v123, v216
	v_min_u32_e32 v215, v123, v216
	v_max_u32_e32 v139, v130, v204
	v_min_u32_e32 v132, v130, v204
	v_max_u32_e32 v124, v127, v145
	v_min_u32_e32 v136, v127, v145
	v_max_u32_e32 v227, v201, v196
	v_min_u32_e32 v220, v201, v196
	v_max_u32_e32 v212, v200, v223
	v_min_u32_e32 v224, v200, v223
	v_max_u32_e32 v125, v217, v214
	v_min_u32_e32 v142, v217, v214
	v_max_u32_e32 v195, v205, v222
	v_min_u32_e32 v131, v205, v222
	v_max_u32_e32 v213, v226, v141
	v_min_u32_e32 v144, v226, v141
	v_max_u32_e32 v197, v218, v215
	v_min_u32_e32 v219, v218, v215
	v_max_u32_e32 v122, v139, v124
	v_min_u32_e32 v199, v139, v124
	v_max_u32_e32 v140, v132, v136
	v_min_u32_e32 v198, v132, v136
	v_max_u32_e32 v133, v227, v212
	v_min_u32_e32 v194, v227, v212
	v_max_u32_e32 v128, v220, v224
	v_min_u32_e32 v135, v220, v224
	v_max_u32_e32 v137, v125, v195
	v_min_u32_e32 v129, v125, v195
	v_max_u32_e32 v225, v142, v131
	v_min_u32_e32 v203, v142, v131
	s_nop 1
	v_max_u32_dpp v202, v203, v213 quad_perm:[1,0,3,2] row_mask:0xf bank_mask:0xf
	v_max_u32_dpp v126, v225, v144 quad_perm:[1,0,3,2] row_mask:0xf bank_mask:0xf
	v_max_u32_dpp v143, v129, v197 quad_perm:[1,0,3,2] row_mask:0xf bank_mask:0xf
	v_max_u32_dpp v134, v137, v219 quad_perm:[1,0,3,2] row_mask:0xf bank_mask:0xf
	v_max_u32_dpp v138, v135, v122 quad_perm:[1,0,3,2] row_mask:0xf bank_mask:0xf
; #define CE_DESC(x, y) do { const unsigned mx_ = (x) > (y) ? (x) : (y); const unsigned mn_ = (x) > (y) ? (y) : (x); (x) = mx_; (y) = mn_; } while (0)
; DI void merge16_desc(unsigned (&a)[16], const unsigned (&b)[16]) {
; #pragma unroll
;   for (int i = 0; i < 16; ++i) a[i] = a[i] > b[15 - i] ? a[i] : b[15 - i];
; #pragma unroll
;   for (int j = 8; j > 0; j >>= 1)
; #pragma unroll
;     for (int i = 0; i < 16; ++i) if ((i & j) == 0) CE_DESC(a[i], a[i + j]);
; }
; template <int CTRL> DI void dpp16(unsigned (&b)[16], const unsigned (&a)[16]) {
; #pragma unroll
;   for (int s = 0; s < 16; ++s) b[s] = (unsigned)__builtin_amdgcn_update_dpp(0, (int)a[s], CTRL, 0xF, 0xF, true);
; }
; DI void peer_select_unit(const Params& p, int unit, char* lds, const bf16x8 (&kb)[4][4]) {
;     ...
;     dpp16<0xB1>(bq, a); merge16_desc(a, bq);
;     dpp16<0x4E>(bq, a); merge16_desc(a, bq);
	v_max_u32_dpp v221, v128, v199 quad_perm:[1,0,3,2] row_mask:0xf bank_mask:0xf
	v_max_u32_dpp v123, v194, v140 quad_perm:[1,0,3,2] row_mask:0xf bank_mask:0xf
	v_max_u32_dpp v216, v133, v198 quad_perm:[1,0,3,2] row_mask:0xf bank_mask:0xf
	v_max_u32_dpp v130, v198, v133 quad_perm:[1,0,3,2] row_mask:0xf bank_mask:0xf
	v_max_u32_dpp v204, v140, v194 quad_perm:[1,0,3,2] row_mask:0xf bank_mask:0xf
	v_max_u32_dpp v127, v199, v128 quad_perm:[1,0,3,2] row_mask:0xf bank_mask:0xf
	v_max_u32_dpp v145, v122, v135 quad_perm:[1,0,3,2] row_mask:0xf bank_mask:0xf
	v_max_u32_dpp v201, v219, v137 quad_perm:[1,0,3,2] row_mask:0xf bank_mask:0xf
	v_max_u32_dpp v196, v197, v129 quad_perm:[1,0,3,2] row_mask:0xf bank_mask:0xf
	v_max_u32_dpp v200, v144, v225 quad_perm:[1,0,3,2] row_mask:0xf bank_mask:0xf
	v_max_u32_dpp v223, v213, v203 quad_perm:[1,0,3,2] row_mask:0xf bank_mask:0xf
	v_max_u32_e32 v217, v202, v130
	v_min_u32_e32 v214, v202, v130
	v_max_u32_e32 v205, v126, v204
	v_min_u32_e32 v222, v126, v204
	v_max_u32_e32 v226, v143, v127
	v_min_u32_e32 v141, v143, v127
	v_max_u32_e32 v218, v134, v145
	v_min_u32_e32 v215, v134, v145
	v_max_u32_e32 v139, v138, v201
	v_min_u32_e32 v124, v138, v201
	v_max_u32_e32 v132, v221, v196
	v_min_u32_e32 v136, v221, v196
	v_max_u32_e32 v227, v123, v200
	v_min_u32_e32 v212, v123, v200
	v_max_u32_e32 v220, v216, v223
	v_min_u32_e32 v224, v216, v223
	v_max_u32_e32 v125, v217, v139
	v_min_u32_e32 v195, v217, v139
	v_max_u32_e32 v142, v205, v132
	v_min_u32_e32 v131, v205, v132
	v_max_u32_e32 v213, v226, v227
	v_min_u32_e32 v144, v226, v227
	v_max_u32_e32 v197, v218, v220
	v_min_u32_e32 v219, v218, v220
	v_max_u32_e32 v122, v214, v124
	v_min_u32_e32 v199, v214, v124
	v_max_u32_e32 v140, v222, v136
	v_min_u32_e32 v198, v222, v136
	v_max_u32_e32 v133, v141, v212
	v_min_u32_e32 v194, v141, v212
	v_max_u32_e32 v128, v215, v224
	v_min_u32_e32 v135, v215, v224
	v_max_u32_e32 v137, v125, v213
	v_min_u32_e32 v129, v125, v213
	v_max_u32_e32 v225, v142, v197
	v_min_u32_e32 v203, v142, v197
	v_max_u32_e32 v202, v195, v144
	v_min_u32_e32 v130, v195, v144
	v_max_u32_e32 v126, v131, v219
	v_min_u32_e32 v204, v131, v219
	v_max_u32_e32 v143, v122, v133
	v_min_u32_e32 v127, v122, v133
	v_max_u32_e32 v134, v140, v128
	v_min_u32_e32 v145, v140, v128
	v_max_u32_e32 v138, v199, v194
	v_min_u32_e32 v201, v199, v194
	v_max_u32_e32 v221, v198, v135
	v_min_u32_e32 v196, v198, v135
	v_max_u32_e32 v123, v137, v225
	v_min_u32_e32 v200, v137, v225
	v_max_u32_e32 v216, v129, v203
	v_min_u32_e32 v223, v129, v203
	v_max_u32_e32 v217, v202, v126
	v_min_u32_e32 v139, v202, v126
	v_max_u32_e32 v205, v130, v204
	v_min_u32_e32 v132, v130, v204
	v_max_u32_e32 v226, v143, v134
	v_min_u32_e32 v227, v143, v134
	v_max_u32_e32 v218, v127, v145
	v_min_u32_e32 v220, v127, v145
	v_max_u32_e32 v214, v138, v221
	v_min_u32_e32 v124, v138, v221
	v_max_u32_e32 v222, v201, v196
	v_min_u32_e32 v136, v201, v196
	s_nop 1
	v_max_u32_dpp v141, v136, v123 quad_perm:[2,3,0,1] row_mask:0xf bank_mask:0xf
	v_max_u32_dpp v212, v222, v200 quad_perm:[2,3,0,1] row_mask:0xf bank_mask:0xf
	v_max_u32_dpp v215, v124, v216 quad_perm:[2,3,0,1] row_mask:0xf bank_mask:0xf
	v_max_u32_dpp v224, v214, v223 quad_perm:[2,3,0,1] row_mask:0xf bank_mask:0xf
	v_max_u32_dpp v125, v220, v217 quad_perm:[2,3,0,1] row_mask:0xf bank_mask:0xf
	v_max_u32_dpp v213, v218, v139 quad_perm:[2,3,0,1] row_mask:0xf bank_mask:0xf
	v_max_u32_dpp v142, v227, v205 quad_perm:[2,3,0,1] row_mask:0xf bank_mask:0xf
	v_max_u32_dpp v197, v226, v132 quad_perm:[2,3,0,1] row_mask:0xf bank_mask:0xf
	v_max_u32_dpp v195, v132, v226 quad_perm:[2,3,0,1] row_mask:0xf bank_mask:0xf
	v_max_u32_dpp v144, v205, v227 quad_perm:[2,3,0,1] row_mask:0xf bank_mask:0xf
	v_max_u32_dpp v131, v139, v218 quad_perm:[2,3,0,1] row_mask:0xf bank_mask:0xf
	v_max_u32_dpp v219, v217, v220 quad_perm:[2,3,0,1] row_mask:0xf bank_mask:0xf
	v_max_u32_dpp v122, v223, v214 quad_perm:[2,3,0,1] row_mask:0xf bank_mask:0xf
	v_max_u32_dpp v133, v216, v124 quad_perm:[2,3,0,1] row_mask:0xf bank_mask:0xf
	v_max_u32_dpp v140, v200, v222 quad_perm:[2,3,0,1] row_mask:0xf bank_mask:0xf
	v_max_u32_dpp v128, v123, v136 quad_perm:[2,3,0,1] row_mask:0xf bank_mask:0xf
	v_max_u32_e32 v199, v141, v195
	v_min_u32_e32 v194, v141, v195
	v_max_u32_e32 v198, v212, v144
	v_min_u32_e32 v135, v212, v144
	v_max_u32_e32 v137, v215, v131
	v_min_u32_e32 v225, v215, v131
	v_max_u32_e32 v129, v224, v219
	v_min_u32_e32 v203, v224, v219
	v_max_u32_e32 v202, v125, v122
	v_min_u32_e32 v126, v125, v122
	v_max_u32_e32 v130, v213, v133
	v_min_u32_e32 v204, v213, v133
	v_max_u32_e32 v143, v142, v140
	v_min_u32_e32 v134, v142, v140
	v_max_u32_e32 v127, v197, v128
	v_min_u32_e32 v145, v197, v128
	v_max_u32_e32 v138, v199, v202
	v_min_u32_e32 v221, v199, v202
	v_max_u32_e32 v201, v198, v130
	v_min_u32_e32 v196, v198, v130
	v_max_u32_e32 v123, v137, v143
	v_min_u32_e32 v200, v137, v143
	v_max_u32_e32 v216, v129, v127
	v_min_u32_e32 v223, v129, v127
	v_max_u32_e32 v217, v194, v126
	v_min_u32_e32 v139, v194, v126
	v_max_u32_e32 v205, v135, v204
	v_min_u32_e32 v132, v135, v204
	v_max_u32_e32 v226, v225, v134
	v_min_u32_e32 v227, v225, v134
	v_max_u32_e32 v218, v203, v145
	v_min_u32_e32 v220, v203, v145
	v_max_u32_e32 v214, v138, v123
	v_min_u32_e32 v124, v138, v123
	v_max_u32_e32 v222, v201, v216
	v_min_u32_e32 v136, v201, v216
	v_max_u32_e32 v141, v221, v200
	v_min_u32_e32 v195, v221, v200
	v_max_u32_e32 v212, v196, v223
	v_min_u32_e32 v144, v196, v223
	v_max_u32_e32 v215, v217, v226
	v_min_u32_e32 v131, v217, v226
	v_max_u32_e32 v224, v205, v218
	v_min_u32_e32 v219, v205, v218
	v_max_u32_e32 v125, v139, v227
; DI void peer_select_unit(const Params& p, int unit, char* lds, const bf16x8 (&kb)[4][4]) {
;     ...
;     dpp16<0x4E>(bq, a); merge16_desc(a, bq);
;     dpp16<0x141>(bq, a); merge16_desc(a, bq);
; #pragma unroll
;     for (int s = 0; s < 2; ++s) {
;       unsigned k = 0u;
; #pragma unroll
;       for (int q = 0; q < 8; ++q) k = part == q ? a[2 * q + s] : k;
;       const int idx = 127 - (int)(k & 127u);
;       topv[rr * 16 + 2 * part + s] = sc[rr * 132 + idx]; topi[rr * 16 + 2 * part + s] = idx;
;     }
;   }
;   __syncthreads();
;   if (tid < 128) {
;     const int tok = tid >> 2, q4 = tid & 3;
;     unsigned c[16], bq[16];
; #pragma unroll
;     for (int i = 0; i < 16; ++i) {
;       const unsigned code = PEER_CAND[16 * q4 + i];
;       const float v = topv[tok * 16 + ((code >> 4) & 15)] + topv[(32 + tok) * 16 + (code & 15)];
	v_min_u32_e32 v122, v139, v227
	v_max_u32_e32 v213, v132, v220
	v_min_u32_e32 v133, v132, v220
	v_max_u32_e32 v142, v214, v222
	v_min_u32_e32 v140, v214, v222
	v_max_u32_e32 v197, v124, v136
	v_min_u32_e32 v128, v124, v136
	v_max_u32_e32 v199, v141, v212
	v_min_u32_e32 v202, v141, v212
	v_max_u32_e32 v198, v195, v144
	v_min_u32_e32 v130, v195, v144
	v_max_u32_e32 v137, v215, v224
	v_min_u32_e32 v143, v215, v224
	v_max_u32_e32 v129, v131, v219
	v_min_u32_e32 v127, v131, v219
	v_max_u32_e32 v194, v125, v213
	v_min_u32_e32 v126, v125, v213
	v_max_u32_e32 v135, v122, v133
	v_min_u32_e32 v204, v122, v133
	v_cmp_eq_u32_e32 vcc, 1, v237
	s_nop 1
	v_cndmask_b32_e32 v225, v142, v199, vcc
	v_cndmask_b32_e32 v134, v140, v202, vcc
	v_cndmask_b32_e32 v203, v197, v198, vcc
	v_cndmask_b32_e32 v145, v128, v130, vcc
	v_cmp_eq_u32_e32 vcc, 2, v237
	s_nop 1
	v_cndmask_b32_e32 v225, v225, v137, vcc
	v_cndmask_b32_e32 v134, v134, v143, vcc
	v_cndmask_b32_e32 v203, v203, v129, vcc
	v_cndmask_b32_e32 v145, v145, v127, vcc
	v_cmp_eq_u32_e32 vcc, 3, v237
	s_nop 1
	v_cndmask_b32_e32 v225, v225, v194, vcc
	v_cndmask_b32_e32 v134, v134, v126, vcc
	v_cndmask_b32_e32 v203, v203, v135, vcc
	v_cndmask_b32_e32 v145, v145, v204, vcc
	v_and_b32_e32 v240, 0x7f, v225
	v_sub_u32_e32 v228, 0x7f, v240
	v_lshl_add_u32 v225, v228, 2, v238
	ds_read_b32 v232, v225
	v_and_b32_e32 v240, 0x7f, v134
	v_sub_u32_e32 v229, 0x7f, v240
	v_lshl_add_u32 v134, v229, 2, v238
	ds_read_b32 v233, v134
	v_and_b32_e32 v240, 0x7f, v203
	v_sub_u32_e32 v230, 0x7f, v240
	v_lshl_add_u32 v203, v230, 2, v238
	ds_read_b32 v234, v203
	v_and_b32_e32 v240, 0x7f, v145
	v_sub_u32_e32 v231, 0x7f, v240
	v_lshl_add_u32 v145, v231, 2, v238
	ds_read_b32 v235, v145
	v_lshlrev_b32_e32 v239, 6, v236
	v_lshl_add_u32 v239, v237, 4, v239
	v_add_u32_e32 v239, v146, v239
	ds_write_b128 v239, v[228:231] offset:37888
	s_waitcnt lgkmcnt(1)
	ds_write_b128 v239, v[232:235] offset:33792
	v_xor_b32_e32 v66, v249, v66
	v_cmp_gt_i32_e32 vcc, s18, v66
	s_waitcnt lgkmcnt(0)
	s_barrier
	s_and_saveexec_b64 s[8:9], vcc
	s_cbranch_execz .LBB0_1651
	v_and_b32_e32 v77, 3, v66
	v_lshrrev_b32_e32 v75, 2, v66
	v_lshlrev_b32_e32 v64, 4, v77
	v_and_b32_e32 v80, 0xffff, v244
	v_lshlrev_b32_e32 v66, 6, v75
	v_lshlrev_b32_e32 v76, 4, v75
	v_cmp_eq_u32_e32 vcc, 3, v77
	v_cmp_ne_u32_e64 s[0:1], 3, v77
	v_mov_b32_e32 v82, 0
	v_lshrrev_b32_e32 v67, 2, v80
	v_and_b32_e32 v68, 15, v80
	v_lshrrev_b16_e32 v79, 8, v80
	v_and_b32_e32 v67, 60, v67
	v_lshlrev_b32_e32 v68, 2, v68
	v_lshrrev_b32_e32 v69, 2, v79
	v_and_b32_e32 v78, 15, v79
	v_add3_u32 v67, v146, v67, v66
	v_add3_u32 v68, v146, v68, v66
	v_and_b32_e32 v69, 60, v69
	v_lshlrev_b32_e32 v78, 2, v78
	v_add3_u32 v81, v146, v69, v66
	v_add3_u32 v78, v146, v78, v66
	ds_read_b32 v67, v67 offset:33792
	ds_read_b32 v69, v68 offset:35840
	ds_read_b32 v66, v81 offset:33792
	ds_read_b32 v68, v78 offset:35840
	v_mov_b32_e32 v81, 0
	v_lshlrev_b32_e32 v78, 2, v76
	v_mov_b32_e32 v83, 0
	v_mov_b32_e32 v84, 0
	v_mov_b32_e32 v85, 0
	v_mov_b32_e32 v86, 0
	v_mov_b32_e32 v87, 0
	v_mov_b32_e32 v88, 0
	v_mov_b32_e32 v89, 0
	v_mov_b32_e32 v90, 0
	v_mov_b32_e32 v91, 0
	v_mov_b32_e32 v92, 0
	v_mov_b32_e32 v93, 0
	v_mov_b32_e32 v94, 0
	s_and_saveexec_b64 s[6:7], s[0:1]
	v_bfe_u32 v82, v244, 16, 8
	v_lshrrev_b32_e32 v238, 2, v82
	v_and_b32_e32 v239, 15, v82
	v_and_b32_e32 v238, 60, v238
	v_lshlrev_b32_e32 v239, 2, v239
	v_add3_u32 v238, v146, v238, v78
	v_add3_u32 v239, v146, v239, v78
	ds_read_b32 v210, v238 offset:33792
	ds_read_b32 v211, v239 offset:35840
	v_bfe_u32 v81, v244, 24, 8
	v_lshrrev_b32_e32 v238, 2, v81
	v_and_b32_e32 v239, 15, v81
	v_and_b32_e32 v238, 60, v238
	v_lshlrev_b32_e32 v239, 2, v239
	v_add3_u32 v238, v146, v238, v78
	v_add3_u32 v239, v146, v239, v78
	ds_read_b32 v212, v238 offset:33792
	ds_read_b32 v213, v239 offset:35840
	v_bfe_u32 v84, v245, 0, 8
	v_lshrrev_b32_e32 v238, 2, v84
	v_and_b32_e32 v239, 15, v84
	v_and_b32_e32 v238, 60, v238
	v_lshlrev_b32_e32 v239, 2, v239
	v_add3_u32 v238, v146, v238, v78
	v_add3_u32 v239, v146, v239, v78
	ds_read_b32 v214, v238 offset:33792
	ds_read_b32 v215, v239 offset:35840
	v_bfe_u32 v83, v245, 8, 8
	v_lshrrev_b32_e32 v238, 2, v83
	v_and_b32_e32 v239, 15, v83
	v_and_b32_e32 v238, 60, v238
	v_lshlrev_b32_e32 v239, 2, v239
	v_add3_u32 v238, v146, v238, v78
	v_add3_u32 v239, v146, v239, v78
	ds_read_b32 v216, v238 offset:33792
	ds_read_b32 v217, v239 offset:35840
	v_bfe_u32 v86, v245, 16, 8
	v_lshrrev_b32_e32 v238, 2, v86
	v_and_b32_e32 v239, 15, v86
	v_and_b32_e32 v238, 60, v238
	v_lshlrev_b32_e32 v239, 2, v239
	v_add3_u32 v238, v146, v238, v78
	v_add3_u32 v239, v146, v239, v78
	ds_read_b32 v218, v238 offset:33792
	ds_read_b32 v219, v239 offset:35840
	v_bfe_u32 v85, v245, 24, 8
	v_lshrrev_b32_e32 v238, 2, v85
	v_and_b32_e32 v239, 15, v85
	v_and_b32_e32 v238, 60, v238
	v_lshlrev_b32_e32 v239, 2, v239
	v_add3_u32 v238, v146, v238, v78
	v_add3_u32 v239, v146, v239, v78
	ds_read_b32 v220, v238 offset:33792
	ds_read_b32 v221, v239 offset:35840
	v_bfe_u32 v88, v246, 0, 8
	v_lshrrev_b32_e32 v238, 2, v88
	v_and_b32_e32 v239, 15, v88
	v_and_b32_e32 v238, 60, v238
	v_lshlrev_b32_e32 v239, 2, v239
	v_add3_u32 v238, v146, v238, v78
	v_add3_u32 v239, v146, v239, v78
	ds_read_b32 v222, v238 offset:33792
	ds_read_b32 v223, v239 offset:35840
	v_bfe_u32 v87, v246, 8, 8
	v_lshrrev_b32_e32 v238, 2, v87
	v_and_b32_e32 v239, 15, v87
	v_and_b32_e32 v238, 60, v238
	v_lshlrev_b32_e32 v239, 2, v239
	v_add3_u32 v238, v146, v238, v78
	v_add3_u32 v239, v146, v239, v78
; DI unsigned ordkey(float f) { const unsigned u = __float_as_uint(f); return (u & 0x80000000u) ? ~u : (u | 0x80000000u); }
; DI void peer_select_unit(const Params& p, int unit, char* lds, const bf16x8 (&kb)[4][4]) {
;     ...
; #pragma unroll
;     for (int i = 0; i < 16; ++i) {
;       const unsigned code = PEER_CAND[16 * q4 + i];
;       const float v = topv[tok * 16 + ((code >> 4) & 15)] + topv[(32 + tok) * 16 + (code & 15)];
;       c[i] = code == 0xFFu ? 0u : ((ordkey(v) & ~255u) | (255u - code));
;     }
	ds_read_b32 v224, v238 offset:33792
	ds_read_b32 v225, v239 offset:35840
	v_bfe_u32 v90, v246, 16, 8
	v_lshrrev_b32_e32 v238, 2, v90
	v_and_b32_e32 v239, 15, v90
	v_and_b32_e32 v238, 60, v238
	v_lshlrev_b32_e32 v239, 2, v239
	v_add3_u32 v238, v146, v238, v78
	v_add3_u32 v239, v146, v239, v78
	ds_read_b32 v226, v238 offset:33792
	ds_read_b32 v227, v239 offset:35840
	v_bfe_u32 v89, v246, 24, 8
	v_lshrrev_b32_e32 v238, 2, v89
	v_and_b32_e32 v239, 15, v89
	v_and_b32_e32 v238, 60, v238
	v_lshlrev_b32_e32 v239, 2, v239
	v_add3_u32 v238, v146, v238, v78
	v_add3_u32 v239, v146, v239, v78
	ds_read_b32 v228, v238 offset:33792
	ds_read_b32 v229, v239 offset:35840
	v_bfe_u32 v92, v247, 0, 8
	v_lshrrev_b32_e32 v238, 2, v92
	v_and_b32_e32 v239, 15, v92
	v_and_b32_e32 v238, 60, v238
	v_lshlrev_b32_e32 v239, 2, v239
	v_add3_u32 v238, v146, v238, v78
	v_add3_u32 v239, v146, v239, v78
	ds_read_b32 v230, v238 offset:33792
	ds_read_b32 v231, v239 offset:35840
	v_bfe_u32 v91, v247, 8, 8
	v_lshrrev_b32_e32 v238, 2, v91
	v_and_b32_e32 v239, 15, v91
	v_and_b32_e32 v238, 60, v238
	v_lshlrev_b32_e32 v239, 2, v239
	v_add3_u32 v238, v146, v238, v78
	v_add3_u32 v239, v146, v239, v78
	ds_read_b32 v232, v238 offset:33792
	ds_read_b32 v233, v239 offset:35840
	v_bfe_u32 v94, v247, 16, 8
	v_lshrrev_b32_e32 v238, 2, v94
	v_and_b32_e32 v239, 15, v94
	v_and_b32_e32 v238, 60, v238
	v_lshlrev_b32_e32 v239, 2, v239
	v_add3_u32 v238, v146, v238, v78
	v_add3_u32 v239, v146, v239, v78
	ds_read_b32 v234, v238 offset:33792
	ds_read_b32 v235, v239 offset:35840
	v_bfe_u32 v70, v247, 24, 8
	v_lshrrev_b32_e32 v238, 2, v70
	v_and_b32_e32 v239, 15, v70
	v_and_b32_e32 v238, 60, v238
	v_lshlrev_b32_e32 v239, 2, v239
	v_add3_u32 v238, v146, v238, v78
	v_add3_u32 v239, v146, v239, v78
	ds_read_b32 v236, v238 offset:33792
	ds_read_b32 v237, v239 offset:35840
	s_waitcnt lgkmcnt(0)
	v_add_f32_e32 v210, v210, v211
	v_cmp_gt_i32_e64 s[4:5], 0, v210
	v_not_b32_e32 v211, v210
	v_or_b32_e32 v238, 0x80000000, v210
	v_cndmask_b32_e64 v210, v238, v211, s[4:5]
	v_and_b32_e32 v210, 0xffffff00, v210
	v_bitop3_b32 v82, v210, s19, v82 bitop3:0x36
	v_add_f32_e32 v212, v212, v213
	v_cmp_gt_i32_e64 s[4:5], 0, v212
	v_not_b32_e32 v213, v212
	v_or_b32_e32 v238, 0x80000000, v212
	v_cndmask_b32_e64 v212, v238, v213, s[4:5]
	v_and_b32_e32 v212, 0xffffff00, v212
	v_bitop3_b32 v81, v212, s19, v81 bitop3:0x36
	v_add_f32_e32 v214, v214, v215
	v_cmp_gt_i32_e64 s[4:5], 0, v214
	v_not_b32_e32 v215, v214
	v_or_b32_e32 v238, 0x80000000, v214
	v_cndmask_b32_e64 v214, v238, v215, s[4:5]
	v_and_b32_e32 v214, 0xffffff00, v214
	v_bitop3_b32 v84, v214, s19, v84 bitop3:0x36
	v_add_f32_e32 v216, v216, v217
	v_cmp_gt_i32_e64 s[4:5], 0, v216
	v_not_b32_e32 v217, v216
	v_or_b32_e32 v238, 0x80000000, v216
	v_cndmask_b32_e64 v216, v238, v217, s[4:5]
	v_and_b32_e32 v216, 0xffffff00, v216
	v_bitop3_b32 v83, v216, s19, v83 bitop3:0x36
	v_add_f32_e32 v218, v218, v219
	v_cmp_gt_i32_e64 s[4:5], 0, v218
	v_not_b32_e32 v219, v218
	v_or_b32_e32 v238, 0x80000000, v218
	v_cndmask_b32_e64 v218, v238, v219, s[4:5]
	v_and_b32_e32 v218, 0xffffff00, v218
	v_bitop3_b32 v86, v218, s19, v86 bitop3:0x36
	v_add_f32_e32 v220, v220, v221
	v_cmp_gt_i32_e64 s[4:5], 0, v220
	v_not_b32_e32 v221, v220
	v_or_b32_e32 v238, 0x80000000, v220
	v_cndmask_b32_e64 v220, v238, v221, s[4:5]
	v_and_b32_e32 v220, 0xffffff00, v220
	v_bitop3_b32 v85, v220, s19, v85 bitop3:0x36
	v_add_f32_e32 v222, v222, v223
	v_cmp_gt_i32_e64 s[4:5], 0, v222
	v_not_b32_e32 v223, v222
	v_or_b32_e32 v238, 0x80000000, v222
	v_cndmask_b32_e64 v222, v238, v223, s[4:5]
	v_and_b32_e32 v222, 0xffffff00, v222
	v_bitop3_b32 v88, v222, s19, v88 bitop3:0x36
	v_add_f32_e32 v224, v224, v225
	v_cmp_gt_i32_e64 s[4:5], 0, v224
	v_not_b32_e32 v225, v224
	v_or_b32_e32 v238, 0x80000000, v224
	v_cndmask_b32_e64 v224, v238, v225, s[4:5]
	v_and_b32_e32 v224, 0xffffff00, v224
	v_bitop3_b32 v87, v224, s19, v87 bitop3:0x36
	v_add_f32_e32 v226, v226, v227
	v_cmp_gt_i32_e64 s[4:5], 0, v226
	v_not_b32_e32 v227, v226
	v_or_b32_e32 v238, 0x80000000, v226
	v_cndmask_b32_e64 v226, v238, v227, s[4:5]
	v_and_b32_e32 v226, 0xffffff00, v226
	v_bitop3_b32 v90, v226, s19, v90 bitop3:0x36
	v_add_f32_e32 v228, v228, v229
	v_cmp_gt_i32_e64 s[4:5], 0, v228
	v_not_b32_e32 v229, v228
	v_or_b32_e32 v238, 0x80000000, v228
	v_cndmask_b32_e64 v228, v238, v229, s[4:5]
	v_and_b32_e32 v228, 0xffffff00, v228
	v_bitop3_b32 v89, v228, s19, v89 bitop3:0x36
	v_add_f32_e32 v230, v230, v231
	v_cmp_gt_i32_e64 s[4:5], 0, v230
	v_not_b32_e32 v231, v230
	v_or_b32_e32 v238, 0x80000000, v230
	v_cndmask_b32_e64 v230, v238, v231, s[4:5]
	v_and_b32_e32 v230, 0xffffff00, v230
	v_bitop3_b32 v92, v230, s19, v92 bitop3:0x36
	v_add_f32_e32 v232, v232, v233
	v_cmp_gt_i32_e64 s[4:5], 0, v232
	v_not_b32_e32 v233, v232
	v_or_b32_e32 v238, 0x80000000, v232
	v_cndmask_b32_e64 v232, v238, v233, s[4:5]
	v_and_b32_e32 v232, 0xffffff00, v232
	v_bitop3_b32 v91, v232, s19, v91 bitop3:0x36
	v_add_f32_e32 v234, v234, v235
	v_cmp_gt_i32_e64 s[4:5], 0, v234
	v_not_b32_e32 v235, v234
	v_or_b32_e32 v238, 0x80000000, v234
	v_cndmask_b32_e64 v234, v238, v235, s[4:5]
	v_and_b32_e32 v234, 0xffffff00, v234
	v_bitop3_b32 v94, v234, s19, v94 bitop3:0x36
	v_add_f32_e32 v236, v236, v237
	v_cmp_gt_i32_e64 s[4:5], 0, v236
	v_not_b32_e32 v237, v236
	v_or_b32_e32 v238, 0x80000000, v236
	v_cndmask_b32_e64 v236, v238, v237, s[4:5]
	v_and_b32_e32 v236, 0xffffff00, v236
	v_bitop3_b32 v93, v236, s19, v70 bitop3:0x36
	s_or_b64 exec, exec, s[6:7]
	s_mov_b64 s[4:5], exec
	s_branch .LBB0_1650
